# 8-phase GEMM K-loops (w_in, w_out, moe2): one LDS-DMA piece of each 6-piece load segment issued between the two MFMA groups of the following compute segment, waits recounted to vmcnt(7)
# speedup vs baseline: 1.0081x; 1.0081x over previous
; #define PG8_STAGE(bufoff, gbase, voff) do { _Pragma("unroll") for (int _i = 0; _i < 2; ++_i) \
;         __builtin_amdgcn_global_load_lds((const unsigned*)((const char*)(gbase) + (voff)[_i]), (LAS unsigned*)(lds + (bufoff) + ldsw + _i * 8192), 16, 0, 0); } while (0)
; #define PG8_WAIT_V(n) asm volatile("s_waitcnt vmcnt(" #n ")" ::: "memory")
; #define PG8_WAIT_L(n) asm volatile("s_waitcnt lgkmcnt(" #n ")" ::: "memory")
; #define PG8_BAR __builtin_amdgcn_s_barrier()
; #define PG8_SCHED __builtin_amdgcn_sched_barrier(0)
; #define PG8_STA_CUR(buf, kb, h) do { if constexpr (GATHER) { PG8_STAGE(buf, gA + (kb), oc[h]); } else { PG8_STAGE(buf, cA + (kb) + (h) * hstep, voffA); } } while (0)
; #define PG8_STA_SEL(buf, kb, h) do { if constexpr (GATHER) { if (last) { PG8_STAGE(buf, gA + (kb), on[h]); } else { PG8_STAGE(buf, gA + (kb), oc[h]); } } else { PG8_STAGE(buf, a2p + (kb) + (h) * hstep, voffA); } } while (0)
; template <class Epi, class Sched, bool GATHER, bool F8 = false>
; __device__ __forceinline__ void gemm_phase(LAS unsigned char* lds, const Gemm g, const Sched& S, const Epi& E, const int tid) {
;     ...
;         for (int t = 0; t < nt; t += 2) {
;             const bool last = (t == nt - 2);
;             int to = t; asm volatile("" : "+s"(to));
;             const size_t k1 = (size_t)(to + 1) * kstep, k2 = last ? 0 : (size_t)(to + 2) * kstep, k3 = k2 + kstep;
;             const char* b2 = last ? nB : cB + (size_t)(to + 2) * kstep; const char* b3 = b2 + kstep;
;             const char* a2p = last ? nA : cA;
;             if constexpr (GATHER) { if (last) { if (has_next) { PG8_AOFF(on, nxt); } else {
; #pragma unroll
;                 for (int h = 0; h < 2; ++h)
; #pragma unroll
;                     for (int i = 0; i < 2; ++i) on[h][i] = oc[h][i]; } } }
;             PG8_LDB(B0, 0, 0); PG8_LDB(B1, 0, 1); PG8_SCHED; PG8_LDA(At, 0, 0); PG8_STA_CUR(PG8_SA(1, 1), k1, 1);
;             PG8_WAIT_V(8); PG8_WAIT_L(0); PG8_BAR; PG8_MMA(0, 0, At, B0); PG8_MMA(0, 1, At, B1); PG8_BAR; PG8_SCHED;
;             PG8_LDA(At, 0, 1); PG8_STAGE(PG8_SB(0, 0), b2, voffB); PG8_STAGE(PG8_SB(0, 1), b2 + hstepB, voffB); PG8_STA_SEL(PG8_SA(0, 0), k2, 0);
;             PG8_WAIT_V(8); PG8_WAIT_L(0); PG8_BAR; PG8_MMA(1, 0, At, B0); PG8_MMA(1, 1, At, B1); PG8_BAR; PG8_SCHED;
.LBB0_268:
	s_add_i32 s47, s34, 2
	s_mov_b32 s62, s47
	s_ashr_i32 s63, s62, 31
	s_lshl_b64 s[62:63], s[62:63], 7
	s_add_u32 s88, s62, 0x100
	s_addc_u32 s87, s63, 0
	s_add_u32 s89, s56, s88
	s_addc_u32 s96, s57, s87
	s_add_i32 s86, 0, 0x10000
	s_cmp_eq_u32 s34, 12
	s_cselect_b64 s[90:91], -1, 0
	s_and_b64 s[34:35], s[90:91], exec
	s_cselect_b32 s35, s37, s96
	s_cselect_b32 s34, s45, s89
	s_cselect_b32 s87, 0, s87
	s_cselect_b32 s88, 0, s88
	s_and_b64 s[90:91], s[42:43], s[90:91]
	s_and_b64 s[90:91], s[90:91], exec
	s_cselect_b32 s89, s49, s59
	s_cselect_b32 s90, s48, s58
	s_add_i32 s91, 0, 0x14000
	v_add_u32_e32 v2, s86, v182
	v_add_u32_e32 v3, s86, v183
	v_add_u32_e32 v6, s91, v182
	v_add_u32_e32 v14, s91, v183
	ds_read_b128 v[18:21], v2
	ds_read_b128 v[26:29], v2 offset:2048
	ds_read_b128 v[22:25], v3
	ds_read_b128 v[30:33], v3 offset:2048
	ds_read_b128 v[2:5], v6
	ds_read_b128 v[10:13], v6 offset:2048
	ds_read_b128 v[6:9], v14
	ds_read_b128 v[14:17], v14 offset:2048
	s_add_u32 s62, s58, s62
	s_addc_u32 s63, s59, s63
	s_add_u32 s62, s62, 0x40080
	s_addc_u32 s63, s63, 0
	v_lshl_add_u64 v[188:189], s[62:63], 0, v[164:165]
	s_add_i32 m0, s53, 0xc000
	ds_read_b128 v[172:175], v185
	ds_read_b128 v[196:199], v185 offset:2048
	ds_read_b128 v[176:179], v186
	ds_read_b128 v[200:203], v186 offset:2048
	ds_read_b128 v[204:207], v185 offset:4096
	ds_read_b128 v[212:215], v185 offset:6144
	ds_read_b128 v[208:211], v186 offset:4096
	ds_read_b128 v[216:219], v186 offset:6144
	global_load_lds_dwordx4 v[188:189], off
	v_lshl_add_u64 v[188:189], s[62:63], 0, v[168:169]
	s_add_i32 m0, s53, 0xe000
	s_nop 0
	global_load_lds_dwordx4 v[188:189], off
	s_waitcnt vmcnt(8)
	s_waitcnt lgkmcnt(0)
	s_barrier
	s_setprio 1
	s_waitcnt lgkmcnt(0)
	v_mfma_scale_f32_16x16x128_f8f6f4 v[158:161], v[18:25], v[172:179], v[158:161], v163, v163 op_sel_hi:[0,0,0]
	v_mfma_scale_f32_16x16x128_f8f6f4 v[154:157], v[26:33], v[172:179], v[154:157], v163, v163 op_sel_hi:[0,0,0]
	v_mfma_scale_f32_16x16x128_f8f6f4 v[146:149], v[18:25], v[196:203], v[146:149], v163, v163 op_sel_hi:[0,0,0]
	v_mfma_scale_f32_16x16x128_f8f6f4 v[138:141], v[26:33], v[196:203], v[138:141], v163, v163 op_sel_hi:[0,0,0]
	v_mfma_scale_f32_16x16x128_f8f6f4 v[130:133], v[18:25], v[204:211], v[130:133], v163, v163 op_sel_hi:[0,0,0]
	v_mfma_scale_f32_16x16x128_f8f6f4 v[122:125], v[26:33], v[204:211], v[122:125], v163, v163 op_sel_hi:[0,0,0]
	v_mfma_scale_f32_16x16x128_f8f6f4 v[114:117], v[18:25], v[212:219], v[114:117], v163, v163 op_sel_hi:[0,0,0]
	v_mfma_scale_f32_16x16x128_f8f6f4 v[106:109], v[26:33], v[212:219], v[106:109], v163, v163 op_sel_hi:[0,0,0]
	s_setprio 0
	s_setprio 1
	v_mfma_scale_f32_16x16x128_f8f6f4 v[150:153], v[2:9], v[172:179], v[150:153], v163, v163 op_sel_hi:[0,0,0]
	v_mfma_scale_f32_16x16x128_f8f6f4 v[142:145], v[10:17], v[172:179], v[142:145], v163, v163 op_sel_hi:[0,0,0]
	v_mfma_scale_f32_16x16x128_f8f6f4 v[134:137], v[2:9], v[196:203], v[134:137], v163, v163 op_sel_hi:[0,0,0]
	v_mfma_scale_f32_16x16x128_f8f6f4 v[126:129], v[10:17], v[196:203], v[126:129], v163, v163 op_sel_hi:[0,0,0]
	v_mfma_scale_f32_16x16x128_f8f6f4 v[118:121], v[2:9], v[204:211], v[118:121], v163, v163 op_sel_hi:[0,0,0]
	v_mfma_scale_f32_16x16x128_f8f6f4 v[110:113], v[10:17], v[204:211], v[110:113], v163, v163 op_sel_hi:[0,0,0]
	v_mfma_scale_f32_16x16x128_f8f6f4 v[102:105], v[2:9], v[212:219], v[102:105], v163, v163 op_sel_hi:[0,0,0]
	v_mfma_scale_f32_16x16x128_f8f6f4 v[98:101], v[10:17], v[212:219], v[98:101], v163, v163 op_sel_hi:[0,0,0]
	s_setprio 0
	s_barrier
	s_add_i32 s62, s86, s74
	v_lshl_add_u64 v[172:173], s[34:35], 0, v[166:167]
	s_mov_b32 m0, s62
	ds_read_b128 v[196:199], v185 offset:16384
	ds_read_b128 v[204:207], v185 offset:18432
	ds_read_b128 v[200:203], v186 offset:16384
	ds_read_b128 v[208:211], v186 offset:18432
	ds_read_b128 v[212:215], v185 offset:20480
	ds_read_b128 v[242:245], v185 offset:22528
	ds_read_b128 v[216:219], v186 offset:20480
	ds_read_b128 v[246:249], v186 offset:22528
	global_load_lds_dwordx4 v[172:173], off
	s_add_i32 m0, s62, 0x2000
	s_add_u32 s62, s34, 0x10000
	v_lshl_add_u64 v[174:175], s[34:35], 0, v[170:171]
	s_addc_u32 s63, s35, 0
	s_add_i32 s86, s91, s74
	global_load_lds_dwordx4 v[174:175], off
	v_lshl_add_u64 v[176:177], s[62:63], 0, v[166:167]
	s_mov_b32 m0, s86
	s_nop 0
	global_load_lds_dwordx4 v[176:177], off
	s_add_i32 m0, s86, 0x2000
	v_lshl_add_u64 v[176:177], s[62:63], 0, v[170:171]
	s_add_u32 s62, s90, s88
	s_addc_u32 s63, s89, s87
	global_load_lds_dwordx4 v[176:177], off
	v_lshl_add_u64 v[176:177], s[62:63], 0, v[164:165]
	s_mov_b32 m0, s53
	v_lshl_add_u64 v[178:179], s[62:63], 0, v[168:169]
	global_load_lds_dwordx4 v[176:177], off
	s_waitcnt vmcnt(7)
	s_waitcnt lgkmcnt(0)
	s_barrier
; #define PG8_WAIT_V(n) asm volatile("s_waitcnt vmcnt(" #n ")" ::: "memory")
; #define PG8_WAIT_L(n) asm volatile("s_waitcnt lgkmcnt(" #n ")" ::: "memory")
; #define PG8_BAR __builtin_amdgcn_s_barrier()
; #define PG8_SCHED __builtin_amdgcn_sched_barrier(0)
; #define PG8_STA_SEL(buf, kb, h) do { if constexpr (GATHER) { if (last) { PG8_STAGE(buf, gA + (kb), on[h]); } else { PG8_STAGE(buf, gA + (kb), oc[h]); } } else { PG8_STAGE(buf, a2p + (kb) + (h) * hstep, voffA); } } while (0)
; template <class Epi, class Sched, bool GATHER, bool F8 = false>
; __device__ __forceinline__ void gemm_phase(LAS unsigned char* lds, const Gemm g, const Sched& S, const Epi& E, const int tid) {
;     ...
;             PG8_WAIT_V(8); PG8_WAIT_L(0); PG8_BAR; PG8_MMA(1, 0, At, B0); PG8_MMA(1, 1, At, B1); PG8_BAR; PG8_SCHED;
;             PG8_LDB(B0, 1, 0); PG8_LDB(B1, 1, 1); PG8_SCHED; PG8_LDA(At, 1, 0); PG8_STA_SEL(PG8_SA(0, 1), k2, 1);
;             PG8_WAIT_V(8); PG8_WAIT_L(0); PG8_BAR; PG8_MMA(0, 0, At, B0); PG8_MMA(0, 1, At, B1); PG8_BAR; PG8_SCHED;
	s_setprio 1
	s_waitcnt lgkmcnt(0)
	v_mfma_scale_f32_16x16x128_f8f6f4 v[94:97], v[18:25], v[196:203], v[94:97], v163, v163 op_sel_hi:[0,0,0]
	v_mfma_scale_f32_16x16x128_f8f6f4 v[90:93], v[26:33], v[196:203], v[90:93], v163, v163 op_sel_hi:[0,0,0]
	v_mfma_scale_f32_16x16x128_f8f6f4 v[82:85], v[18:25], v[204:211], v[82:85], v163, v163 op_sel_hi:[0,0,0]
	v_mfma_scale_f32_16x16x128_f8f6f4 v[74:77], v[26:33], v[204:211], v[74:77], v163, v163 op_sel_hi:[0,0,0]
	v_mfma_scale_f32_16x16x128_f8f6f4 v[66:69], v[18:25], v[212:219], v[66:69], v163, v163 op_sel_hi:[0,0,0]
	v_mfma_scale_f32_16x16x128_f8f6f4 v[58:61], v[26:33], v[212:219], v[58:61], v163, v163 op_sel_hi:[0,0,0]
	v_mfma_scale_f32_16x16x128_f8f6f4 v[50:53], v[18:25], v[242:249], v[50:53], v163, v163 op_sel_hi:[0,0,0]
	v_mfma_scale_f32_16x16x128_f8f6f4 v[42:45], v[26:33], v[242:249], v[42:45], v163, v163 op_sel_hi:[0,0,0]
	s_setprio 0
	s_mov_b32 m0, s55
	s_nop 0
	global_load_lds_dwordx4 v[178:179], off
	s_setprio 1
	v_mfma_scale_f32_16x16x128_f8f6f4 v[86:89], v[2:9], v[196:203], v[86:89], v163, v163 op_sel_hi:[0,0,0]
	v_mfma_scale_f32_16x16x128_f8f6f4 v[78:81], v[10:17], v[196:203], v[78:81], v163, v163 op_sel_hi:[0,0,0]
	v_mfma_scale_f32_16x16x128_f8f6f4 v[70:73], v[2:9], v[204:211], v[70:73], v163, v163 op_sel_hi:[0,0,0]
	v_mfma_scale_f32_16x16x128_f8f6f4 v[62:65], v[10:17], v[204:211], v[62:65], v163, v163 op_sel_hi:[0,0,0]
	v_mfma_scale_f32_16x16x128_f8f6f4 v[54:57], v[2:9], v[212:219], v[54:57], v163, v163 op_sel_hi:[0,0,0]
	v_mfma_scale_f32_16x16x128_f8f6f4 v[46:49], v[10:17], v[212:219], v[46:49], v163, v163 op_sel_hi:[0,0,0]
	v_mfma_scale_f32_16x16x128_f8f6f4 v[38:41], v[2:9], v[242:249], v[38:41], v163, v163 op_sel_hi:[0,0,0]
	v_mfma_scale_f32_16x16x128_f8f6f4 v[34:37], v[10:17], v[242:249], v[34:37], v163, v163 op_sel_hi:[0,0,0]
	s_setprio 0
	s_barrier
	s_add_i32 s86, 0, 0x18000
	s_add_i32 s87, 0, 0x1c000
	v_add_u32_e32 v6, s86, v182
	v_add_u32_e32 v14, s86, v183
	v_add_u32_e32 v22, s87, v182
	v_add_u32_e32 v30, s87, v183
	ds_read_b128 v[2:5], v6
	ds_read_b128 v[10:13], v6 offset:2048
	ds_read_b128 v[6:9], v14
	ds_read_b128 v[14:17], v14 offset:2048
	ds_read_b128 v[18:21], v22
	ds_read_b128 v[26:29], v22 offset:2048
	ds_read_b128 v[22:25], v30
	ds_read_b128 v[30:33], v30 offset:2048
	s_add_u32 s62, s62, 0x40000
	s_addc_u32 s63, s63, 0
	s_mov_b32 m0, s75
	v_lshl_add_u64 v[188:189], s[62:63], 0, v[164:165]
	ds_read_b128 v[196:199], v185 offset:32768
	ds_read_b128 v[204:207], v185 offset:34816
	ds_read_b128 v[200:203], v186 offset:32768
	ds_read_b128 v[208:211], v186 offset:34816
	ds_read_b128 v[212:215], v185 offset:36864
	ds_read_b128 v[242:245], v185 offset:38912
	ds_read_b128 v[216:219], v186 offset:36864
	ds_read_b128 v[246:249], v186 offset:38912
	global_load_lds_dwordx4 v[188:189], off
	v_lshl_add_u64 v[188:189], s[62:63], 0, v[168:169]
	s_mov_b32 m0, s80
	s_nop 0
	global_load_lds_dwordx4 v[188:189], off
	s_waitcnt vmcnt(8)
	s_waitcnt lgkmcnt(0)
	s_barrier
	s_setprio 1
	s_waitcnt lgkmcnt(0)
	v_mfma_scale_f32_16x16x128_f8f6f4 v[158:161], v[2:9], v[196:203], v[158:161], v163, v163 op_sel_hi:[0,0,0]
	v_mfma_scale_f32_16x16x128_f8f6f4 v[154:157], v[10:17], v[196:203], v[154:157], v163, v163 op_sel_hi:[0,0,0]
	v_mfma_scale_f32_16x16x128_f8f6f4 v[146:149], v[2:9], v[204:211], v[146:149], v163, v163 op_sel_hi:[0,0,0]
	v_mfma_scale_f32_16x16x128_f8f6f4 v[138:141], v[10:17], v[204:211], v[138:141], v163, v163 op_sel_hi:[0,0,0]
	v_mfma_scale_f32_16x16x128_f8f6f4 v[130:133], v[2:9], v[212:219], v[130:133], v163, v163 op_sel_hi:[0,0,0]
	v_mfma_scale_f32_16x16x128_f8f6f4 v[122:125], v[10:17], v[212:219], v[122:125], v163, v163 op_sel_hi:[0,0,0]
	v_mfma_scale_f32_16x16x128_f8f6f4 v[114:117], v[2:9], v[242:249], v[114:117], v163, v163 op_sel_hi:[0,0,0]
	v_mfma_scale_f32_16x16x128_f8f6f4 v[106:109], v[10:17], v[242:249], v[106:109], v163, v163 op_sel_hi:[0,0,0]
	s_setprio 0
	s_setprio 1
	v_mfma_scale_f32_16x16x128_f8f6f4 v[150:153], v[18:25], v[196:203], v[150:153], v163, v163 op_sel_hi:[0,0,0]
	v_mfma_scale_f32_16x16x128_f8f6f4 v[142:145], v[26:33], v[196:203], v[142:145], v163, v163 op_sel_hi:[0,0,0]
	v_mfma_scale_f32_16x16x128_f8f6f4 v[134:137], v[18:25], v[204:211], v[134:137], v163, v163 op_sel_hi:[0,0,0]
	v_mfma_scale_f32_16x16x128_f8f6f4 v[126:129], v[26:33], v[204:211], v[126:129], v163, v163 op_sel_hi:[0,0,0]
	v_mfma_scale_f32_16x16x128_f8f6f4 v[118:121], v[18:25], v[212:219], v[118:121], v163, v163 op_sel_hi:[0,0,0]
	v_mfma_scale_f32_16x16x128_f8f6f4 v[110:113], v[26:33], v[212:219], v[110:113], v163, v163 op_sel_hi:[0,0,0]
	v_mfma_scale_f32_16x16x128_f8f6f4 v[102:105], v[18:25], v[242:249], v[102:105], v163, v163 op_sel_hi:[0,0,0]
	v_mfma_scale_f32_16x16x128_f8f6f4 v[98:101], v[26:33], v[242:249], v[98:101], v163, v163 op_sel_hi:[0,0,0]
	s_setprio 0
	s_barrier
; #define PG8_STAGE(bufoff, gbase, voff) do { _Pragma("unroll") for (int _i = 0; _i < 2; ++_i) \
;         __builtin_amdgcn_global_load_lds((const unsigned*)((const char*)(gbase) + (voff)[_i]), (LAS unsigned*)(lds + (bufoff) + ldsw + _i * 8192), 16, 0, 0); } while (0)
; #define PG8_WAIT_V(n) asm volatile("s_waitcnt vmcnt(" #n ")" ::: "memory")
; #define PG8_WAIT_L(n) asm volatile("s_waitcnt lgkmcnt(" #n ")" ::: "memory")
; #define PG8_BAR __builtin_amdgcn_s_barrier()
; #define PG8_SCHED __builtin_amdgcn_sched_barrier(0)
; #define PG8_STA_SEL(buf, kb, h) do { if constexpr (GATHER) { if (last) { PG8_STAGE(buf, gA + (kb), on[h]); } else { PG8_STAGE(buf, gA + (kb), oc[h]); } } else { PG8_STAGE(buf, a2p + (kb) + (h) * hstep, voffA); } } while (0)
; template <class Epi, class Sched, bool GATHER, bool F8 = false>
; __device__ __forceinline__ void gemm_phase(LAS unsigned char* lds, const Gemm g, const Sched& S, const Epi& E, const int tid) {
;     ...
;             PG8_LDA(At, 1, 1); PG8_STAGE(PG8_SB(1, 0), b3, voffB); PG8_STAGE(PG8_SB(1, 1), b3 + hstepB, voffB); PG8_STA_SEL(PG8_SA(1, 0), k3, 0);
;             PG8_WAIT_V(8); PG8_WAIT_L(0); PG8_BAR; PG8_MMA(1, 0, At, B0); PG8_MMA(1, 1, At, B1); PG8_BAR; PG8_SCHED;
;         }
;         if (wr == 0) PG8_BAR;
	s_add_i32 s62, s86, s74
	v_lshl_add_u64 v[172:173], v[172:173], 0, s[24:25]
	s_mov_b32 m0, s62
	ds_read_b128 v[196:199], v185 offset:49152
	ds_read_b128 v[204:207], v185 offset:51200
	ds_read_b128 v[200:203], v186 offset:49152
	ds_read_b128 v[208:211], v186 offset:51200
	ds_read_b128 v[212:215], v185 offset:53248
	ds_read_b128 v[242:245], v185 offset:55296
	ds_read_b128 v[216:219], v186 offset:53248
	ds_read_b128 v[246:249], v186 offset:55296
	global_load_lds_dwordx4 v[172:173], off
	s_add_i32 m0, s62, 0x2000
	s_add_u32 s34, s34, 0x10080
	v_lshl_add_u64 v[172:173], v[174:175], 0, s[24:25]
	s_addc_u32 s35, s35, 0
	s_add_i32 s62, s87, s74
	global_load_lds_dwordx4 v[172:173], off
	v_lshl_add_u64 v[172:173], s[34:35], 0, v[166:167]
	s_mov_b32 m0, s62
	s_nop 0
	global_load_lds_dwordx4 v[172:173], off
	v_lshl_add_u64 v[172:173], s[34:35], 0, v[170:171]
	s_add_i32 m0, s62, 0x2000
	s_nop 0
	global_load_lds_dwordx4 v[172:173], off
	v_lshl_add_u64 v[172:173], v[176:177], 0, s[24:25]
	s_mov_b32 m0, s81
	s_nop 0
	global_load_lds_dwordx4 v[172:173], off
	s_waitcnt vmcnt(7)
	s_waitcnt lgkmcnt(0)
	s_barrier
	s_setprio 1
	s_waitcnt lgkmcnt(0)
	v_mfma_scale_f32_16x16x128_f8f6f4 v[94:97], v[2:9], v[196:203], v[94:97], v163, v163 op_sel_hi:[0,0,0]
	v_mfma_scale_f32_16x16x128_f8f6f4 v[90:93], v[10:17], v[196:203], v[90:93], v163, v163 op_sel_hi:[0,0,0]
	v_mfma_scale_f32_16x16x128_f8f6f4 v[82:85], v[2:9], v[204:211], v[82:85], v163, v163 op_sel_hi:[0,0,0]
	v_mfma_scale_f32_16x16x128_f8f6f4 v[74:77], v[10:17], v[204:211], v[74:77], v163, v163 op_sel_hi:[0,0,0]
	v_mfma_scale_f32_16x16x128_f8f6f4 v[66:69], v[2:9], v[212:219], v[66:69], v163, v163 op_sel_hi:[0,0,0]
	v_mfma_scale_f32_16x16x128_f8f6f4 v[58:61], v[10:17], v[212:219], v[58:61], v163, v163 op_sel_hi:[0,0,0]
	v_mfma_scale_f32_16x16x128_f8f6f4 v[50:53], v[2:9], v[242:249], v[50:53], v163, v163 op_sel_hi:[0,0,0]
	v_mfma_scale_f32_16x16x128_f8f6f4 v[42:45], v[10:17], v[242:249], v[42:45], v163, v163 op_sel_hi:[0,0,0]
	s_setprio 0
	v_lshl_add_u64 v[172:173], v[178:179], 0, s[24:25]
	s_mov_b32 m0, s84
	s_nop 0
	global_load_lds_dwordx4 v[172:173], off
	s_setprio 1
	v_mfma_scale_f32_16x16x128_f8f6f4 v[86:89], v[18:25], v[196:203], v[86:89], v163, v163 op_sel_hi:[0,0,0]
	v_mfma_scale_f32_16x16x128_f8f6f4 v[78:81], v[26:33], v[196:203], v[78:81], v163, v163 op_sel_hi:[0,0,0]
	v_mfma_scale_f32_16x16x128_f8f6f4 v[70:73], v[18:25], v[204:211], v[70:73], v163, v163 op_sel_hi:[0,0,0]
	v_mfma_scale_f32_16x16x128_f8f6f4 v[62:65], v[26:33], v[204:211], v[62:65], v163, v163 op_sel_hi:[0,0,0]
	v_mfma_scale_f32_16x16x128_f8f6f4 v[54:57], v[18:25], v[212:219], v[54:57], v163, v163 op_sel_hi:[0,0,0]
	v_mfma_scale_f32_16x16x128_f8f6f4 v[46:49], v[26:33], v[212:219], v[46:49], v163, v163 op_sel_hi:[0,0,0]
	v_mfma_scale_f32_16x16x128_f8f6f4 v[38:41], v[18:25], v[242:249], v[38:41], v163, v163 op_sel_hi:[0,0,0]
	v_mfma_scale_f32_16x16x128_f8f6f4 v[34:37], v[26:33], v[242:249], v[34:37], v163, v163 op_sel_hi:[0,0,0]
	s_setprio 0
	s_barrier
	s_cmp_gt_u32 s47, 13
	s_mov_b32 s34, s47
	s_cbranch_scc0 .LBB0_268
	s_and_b64 vcc, exec, s[40:41]
	s_cbranch_vccz .LBB0_271
	s_barrier

; #define PG8_STAGE(bufoff, gbase, voff) do { _Pragma("unroll") for (int _i = 0; _i < 2; ++_i) \
;         __builtin_amdgcn_global_load_lds((const unsigned*)((const char*)(gbase) + (voff)[_i]), (LAS unsigned*)(lds + (bufoff) + ldsw + _i * 8192), 16, 0, 0); } while (0)
; #define PG8_WAIT_V(n) asm volatile("s_waitcnt vmcnt(" #n ")" ::: "memory")
; #define PG8_WAIT_L(n) asm volatile("s_waitcnt lgkmcnt(" #n ")" ::: "memory")
; #define PG8_BAR __builtin_amdgcn_s_barrier()
; #define PG8_SCHED __builtin_amdgcn_sched_barrier(0)
; #define PG8_STA_CUR(buf, kb, h) do { if constexpr (GATHER) { PG8_STAGE(buf, gA + (kb), oc[h]); } else { PG8_STAGE(buf, cA + (kb) + (h) * hstep, voffA); } } while (0)
; template <class Epi, class Sched, bool GATHER, bool F8 = false>
; __device__ __forceinline__ void gemm_phase(LAS unsigned char* lds, const Gemm g, const Sched& S, const Epi& E, const int tid) {
;     ...
;         for (int t = 0; t < nt; t += 2) {
;             const bool last = (t == nt - 2);
;             int to = t; asm volatile("" : "+s"(to));
;             const size_t k1 = (size_t)(to + 1) * kstep, k2 = last ? 0 : (size_t)(to + 2) * kstep, k3 = k2 + kstep;
;             const char* b2 = last ? nB : cB + (size_t)(to + 2) * kstep; const char* b3 = b2 + kstep;
;             const char* a2p = last ? nA : cA;
;             if constexpr (GATHER) { if (last) { if (has_next) { PG8_AOFF(on, nxt); } else {
; #pragma unroll
;                 for (int h = 0; h < 2; ++h)
; #pragma unroll
;                     for (int i = 0; i < 2; ++i) on[h][i] = oc[h][i]; } } }
;             PG8_LDB(B0, 0, 0); PG8_LDB(B1, 0, 1); PG8_SCHED; PG8_LDA(At, 0, 0); PG8_STA_CUR(PG8_SA(1, 1), k1, 1);
;             PG8_WAIT_V(8); PG8_WAIT_L(0); PG8_BAR; PG8_MMA(0, 0, At, B0); PG8_MMA(0, 1, At, B1); PG8_BAR; PG8_SCHED;
;             PG8_LDA(At, 0, 1); PG8_STAGE(PG8_SB(0, 0), b2, voffB); PG8_STAGE(PG8_SB(0, 1), b2 + hstepB, voffB); PG8_STA_SEL(PG8_SA(0, 0), k2, 0);
;             PG8_WAIT_V(8); PG8_WAIT_L(0); PG8_BAR; PG8_MMA(1, 0, At, B0); PG8_MMA(1, 1, At, B1); PG8_BAR; PG8_SCHED;
;             PG8_LDB(B0, 1, 0); PG8_LDB(B1, 1, 1); PG8_SCHED; PG8_LDA(At, 1, 0); PG8_STA_SEL(PG8_SA(0, 1), k2, 1);
;             PG8_WAIT_V(8); PG8_WAIT_L(0); PG8_BAR; PG8_MMA(0, 0, At, B0); PG8_MMA(0, 1, At, B1); PG8_BAR; PG8_SCHED;
.LBB0_920:
	s_add_i32 s47, s34, 2
	s_mov_b32 s62, s47
	s_ashr_i32 s63, s62, 31
	s_lshl_b64 s[62:63], s[62:63], 7
	s_add_u32 s87, s62, 0x100
	s_addc_u32 s86, s63, 0
	s_add_u32 s90, s56, s87
	s_addc_u32 s91, s57, s86
	s_add_i32 s85, 0, 0x10000
	s_cmp_eq_u32 s34, 12
	s_cselect_b64 s[88:89], -1, 0
	s_and_b64 s[34:35], s[88:89], exec
	s_cselect_b32 s35, s37, s91
	s_cselect_b32 s34, s45, s90
	s_cselect_b32 s86, 0, s86
	s_cselect_b32 s87, 0, s87
	s_and_b64 s[88:89], s[42:43], s[88:89]
	s_and_b64 s[88:89], s[88:89], exec
	s_cselect_b32 s88, s49, s59
	s_cselect_b32 s89, s48, s58
	s_add_i32 s90, 0, 0x14000
	v_add_u32_e32 v2, s85, v179
	v_add_u32_e32 v3, s85, v180
	v_add_u32_e32 v6, s90, v179
	v_add_u32_e32 v14, s90, v180
	ds_read_b128 v[18:21], v2
	ds_read_b128 v[26:29], v2 offset:2048
	ds_read_b128 v[22:25], v3
	ds_read_b128 v[30:33], v3 offset:2048
	ds_read_b128 v[2:5], v6
	ds_read_b128 v[10:13], v6 offset:2048
	ds_read_b128 v[6:9], v14
	ds_read_b128 v[14:17], v14 offset:2048
	s_add_u32 s62, s58, s62
	s_addc_u32 s63, s59, s63
	s_add_u32 s62, s62, 0x40080
	s_addc_u32 s63, s63, 0
	v_lshl_add_u64 v[192:193], s[62:63], 0, v[162:163]
	s_add_i32 m0, s53, 0xc000
	ds_read_b128 v[170:173], v182
	ds_read_b128 v[184:187], v182 offset:2048
	ds_read_b128 v[174:177], v183
	ds_read_b128 v[188:191], v183 offset:2048
	ds_read_b128 v[196:199], v182 offset:4096
	ds_read_b128 v[204:207], v182 offset:6144
	ds_read_b128 v[200:203], v183 offset:4096
	ds_read_b128 v[208:211], v183 offset:6144
	global_load_lds_dwordx4 v[192:193], off
	v_lshl_add_u64 v[192:193], s[62:63], 0, v[166:167]
	s_add_i32 m0, s53, 0xe000
	s_nop 0
	global_load_lds_dwordx4 v[192:193], off
	s_waitcnt vmcnt(8)
	s_waitcnt lgkmcnt(0)
	s_barrier
	s_setprio 1
	s_waitcnt lgkmcnt(0)
	v_mfma_scale_f32_16x16x128_f8f6f4 v[158:161], v[18:25], v[170:177], v[158:161], v1, v1 op_sel_hi:[0,0,0]
	v_mfma_scale_f32_16x16x128_f8f6f4 v[154:157], v[26:33], v[170:177], v[154:157], v1, v1 op_sel_hi:[0,0,0]
	v_mfma_scale_f32_16x16x128_f8f6f4 v[142:145], v[18:25], v[184:191], v[142:145], v1, v1 op_sel_hi:[0,0,0]
	v_mfma_scale_f32_16x16x128_f8f6f4 v[138:141], v[26:33], v[184:191], v[138:141], v1, v1 op_sel_hi:[0,0,0]
	v_mfma_scale_f32_16x16x128_f8f6f4 v[126:129], v[18:25], v[196:203], v[126:129], v1, v1 op_sel_hi:[0,0,0]
	v_mfma_scale_f32_16x16x128_f8f6f4 v[122:125], v[26:33], v[196:203], v[122:125], v1, v1 op_sel_hi:[0,0,0]
	v_mfma_scale_f32_16x16x128_f8f6f4 v[110:113], v[18:25], v[204:211], v[110:113], v1, v1 op_sel_hi:[0,0,0]
	v_mfma_scale_f32_16x16x128_f8f6f4 v[106:109], v[26:33], v[204:211], v[106:109], v1, v1 op_sel_hi:[0,0,0]
	s_setprio 0
	s_setprio 1
	v_mfma_scale_f32_16x16x128_f8f6f4 v[150:153], v[2:9], v[170:177], v[150:153], v1, v1 op_sel_hi:[0,0,0]
	v_mfma_scale_f32_16x16x128_f8f6f4 v[146:149], v[10:17], v[170:177], v[146:149], v1, v1 op_sel_hi:[0,0,0]
	v_mfma_scale_f32_16x16x128_f8f6f4 v[134:137], v[2:9], v[184:191], v[134:137], v1, v1 op_sel_hi:[0,0,0]
	v_mfma_scale_f32_16x16x128_f8f6f4 v[130:133], v[10:17], v[184:191], v[130:133], v1, v1 op_sel_hi:[0,0,0]
	v_mfma_scale_f32_16x16x128_f8f6f4 v[118:121], v[2:9], v[196:203], v[118:121], v1, v1 op_sel_hi:[0,0,0]
	v_mfma_scale_f32_16x16x128_f8f6f4 v[114:117], v[10:17], v[196:203], v[114:117], v1, v1 op_sel_hi:[0,0,0]
	v_mfma_scale_f32_16x16x128_f8f6f4 v[102:105], v[2:9], v[204:211], v[102:105], v1, v1 op_sel_hi:[0,0,0]
	v_mfma_scale_f32_16x16x128_f8f6f4 v[98:101], v[10:17], v[204:211], v[98:101], v1, v1 op_sel_hi:[0,0,0]
	s_setprio 0
	s_barrier
	s_add_i32 s62, s85, s60
	v_lshl_add_u64 v[170:171], s[34:35], 0, v[164:165]
	s_mov_b32 m0, s62
	ds_read_b128 v[184:187], v182 offset:16384
	ds_read_b128 v[196:199], v182 offset:18432
	ds_read_b128 v[188:191], v183 offset:16384
	ds_read_b128 v[200:203], v183 offset:18432
	ds_read_b128 v[204:207], v182 offset:20480
	ds_read_b128 v[212:215], v182 offset:22528
	ds_read_b128 v[208:211], v183 offset:20480
	ds_read_b128 v[216:219], v183 offset:22528
	global_load_lds_dwordx4 v[170:171], off
	s_add_i32 m0, s62, 0x2000
	s_add_u32 s62, s34, 0x40000
	v_lshl_add_u64 v[172:173], s[34:35], 0, v[168:169]
	s_addc_u32 s63, s35, 0
	s_add_i32 s85, s90, s60
	global_load_lds_dwordx4 v[172:173], off
	v_lshl_add_u64 v[174:175], s[62:63], 0, v[164:165]
	s_mov_b32 m0, s85
	s_nop 0
	global_load_lds_dwordx4 v[174:175], off
	s_add_i32 m0, s85, 0x2000
	v_lshl_add_u64 v[174:175], s[62:63], 0, v[168:169]
	s_add_u32 s62, s89, s87
	s_addc_u32 s63, s88, s86
	global_load_lds_dwordx4 v[174:175], off
	v_lshl_add_u64 v[174:175], s[62:63], 0, v[162:163]
	s_mov_b32 m0, s53
	v_lshl_add_u64 v[176:177], s[62:63], 0, v[166:167]
	global_load_lds_dwordx4 v[174:175], off
	s_waitcnt vmcnt(7)
	s_waitcnt lgkmcnt(0)
	s_barrier
	s_setprio 1
	s_waitcnt lgkmcnt(0)
	v_mfma_scale_f32_16x16x128_f8f6f4 v[94:97], v[18:25], v[184:191], v[94:97], v1, v1 op_sel_hi:[0,0,0]
	v_mfma_scale_f32_16x16x128_f8f6f4 v[90:93], v[26:33], v[184:191], v[90:93], v1, v1 op_sel_hi:[0,0,0]
	v_mfma_scale_f32_16x16x128_f8f6f4 v[78:81], v[18:25], v[196:203], v[78:81], v1, v1 op_sel_hi:[0,0,0]
	v_mfma_scale_f32_16x16x128_f8f6f4 v[74:77], v[26:33], v[196:203], v[74:77], v1, v1 op_sel_hi:[0,0,0]
	v_mfma_scale_f32_16x16x128_f8f6f4 v[62:65], v[18:25], v[204:211], v[62:65], v1, v1 op_sel_hi:[0,0,0]
	v_mfma_scale_f32_16x16x128_f8f6f4 v[58:61], v[26:33], v[204:211], v[58:61], v1, v1 op_sel_hi:[0,0,0]
	v_mfma_scale_f32_16x16x128_f8f6f4 v[46:49], v[18:25], v[212:219], v[46:49], v1, v1 op_sel_hi:[0,0,0]
	v_mfma_scale_f32_16x16x128_f8f6f4 v[42:45], v[26:33], v[212:219], v[42:45], v1, v1 op_sel_hi:[0,0,0]
	s_setprio 0
	s_mov_b32 m0, s55
	s_nop 0
	global_load_lds_dwordx4 v[176:177], off
	s_setprio 1
	v_mfma_scale_f32_16x16x128_f8f6f4 v[86:89], v[2:9], v[184:191], v[86:89], v1, v1 op_sel_hi:[0,0,0]
	v_mfma_scale_f32_16x16x128_f8f6f4 v[82:85], v[10:17], v[184:191], v[82:85], v1, v1 op_sel_hi:[0,0,0]
	v_mfma_scale_f32_16x16x128_f8f6f4 v[70:73], v[2:9], v[196:203], v[70:73], v1, v1 op_sel_hi:[0,0,0]
	v_mfma_scale_f32_16x16x128_f8f6f4 v[66:69], v[10:17], v[196:203], v[66:69], v1, v1 op_sel_hi:[0,0,0]
	v_mfma_scale_f32_16x16x128_f8f6f4 v[54:57], v[2:9], v[204:211], v[54:57], v1, v1 op_sel_hi:[0,0,0]
	v_mfma_scale_f32_16x16x128_f8f6f4 v[50:53], v[10:17], v[204:211], v[50:53], v1, v1 op_sel_hi:[0,0,0]
	v_mfma_scale_f32_16x16x128_f8f6f4 v[38:41], v[2:9], v[212:219], v[38:41], v1, v1 op_sel_hi:[0,0,0]
	v_mfma_scale_f32_16x16x128_f8f6f4 v[34:37], v[10:17], v[212:219], v[34:37], v1, v1 op_sel_hi:[0,0,0]
	s_setprio 0
	s_barrier
; #define PG8_STAGE(bufoff, gbase, voff) do { _Pragma("unroll") for (int _i = 0; _i < 2; ++_i) \
;         __builtin_amdgcn_global_load_lds((const unsigned*)((const char*)(gbase) + (voff)[_i]), (LAS unsigned*)(lds + (bufoff) + ldsw + _i * 8192), 16, 0, 0); } while (0)
; #define PG8_WAIT_V(n) asm volatile("s_waitcnt vmcnt(" #n ")" ::: "memory")
; #define PG8_WAIT_L(n) asm volatile("s_waitcnt lgkmcnt(" #n ")" ::: "memory")
; #define PG8_BAR __builtin_amdgcn_s_barrier()
; #define PG8_SCHED __builtin_amdgcn_sched_barrier(0)
; #define PG8_STA_SEL(buf, kb, h) do { if constexpr (GATHER) { if (last) { PG8_STAGE(buf, gA + (kb), on[h]); } else { PG8_STAGE(buf, gA + (kb), oc[h]); } } else { PG8_STAGE(buf, a2p + (kb) + (h) * hstep, voffA); } } while (0)
; template <class Epi, class Sched, bool GATHER, bool F8 = false>
; __device__ __forceinline__ void gemm_phase(LAS unsigned char* lds, const Gemm g, const Sched& S, const Epi& E, const int tid) {
;     ...
;             PG8_LDB(B0, 1, 0); PG8_LDB(B1, 1, 1); PG8_SCHED; PG8_LDA(At, 1, 0); PG8_STA_SEL(PG8_SA(0, 1), k2, 1);
;             PG8_WAIT_V(8); PG8_WAIT_L(0); PG8_BAR; PG8_MMA(0, 0, At, B0); PG8_MMA(0, 1, At, B1); PG8_BAR; PG8_SCHED;
;             PG8_LDA(At, 1, 1); PG8_STAGE(PG8_SB(1, 0), b3, voffB); PG8_STAGE(PG8_SB(1, 1), b3 + hstepB, voffB); PG8_STA_SEL(PG8_SA(1, 0), k3, 0);
;             PG8_WAIT_V(8); PG8_WAIT_L(0); PG8_BAR; PG8_MMA(1, 0, At, B0); PG8_MMA(1, 1, At, B1); PG8_BAR; PG8_SCHED;
;         }
;         if (wr == 0) PG8_BAR;
	s_add_i32 s85, 0, 0x18000
	s_add_i32 s86, 0, 0x1c000
	v_add_u32_e32 v6, s85, v179
	v_add_u32_e32 v14, s85, v180
	v_add_u32_e32 v22, s86, v179
	v_add_u32_e32 v30, s86, v180
	ds_read_b128 v[2:5], v6
	ds_read_b128 v[10:13], v6 offset:2048
	ds_read_b128 v[6:9], v14
	ds_read_b128 v[14:17], v14 offset:2048
	ds_read_b128 v[18:21], v22
	ds_read_b128 v[26:29], v22 offset:2048
	ds_read_b128 v[22:25], v30
	ds_read_b128 v[30:33], v30 offset:2048
	s_add_u32 s62, s62, 0x40000
	s_addc_u32 s63, s63, 0
	s_mov_b32 m0, s72
	v_lshl_add_u64 v[192:193], s[62:63], 0, v[162:163]
	ds_read_b128 v[184:187], v182 offset:32768
	ds_read_b128 v[196:199], v182 offset:34816
	ds_read_b128 v[188:191], v183 offset:32768
	ds_read_b128 v[200:203], v183 offset:34816
	ds_read_b128 v[204:207], v182 offset:36864
	ds_read_b128 v[212:215], v182 offset:38912
	ds_read_b128 v[208:211], v183 offset:36864
	ds_read_b128 v[216:219], v183 offset:38912
	global_load_lds_dwordx4 v[192:193], off
	v_lshl_add_u64 v[192:193], s[62:63], 0, v[166:167]
	s_mov_b32 m0, s73
	s_nop 0
	global_load_lds_dwordx4 v[192:193], off
	s_waitcnt vmcnt(8)
	s_waitcnt lgkmcnt(0)
	s_barrier
	s_setprio 1
	s_waitcnt lgkmcnt(0)
	v_mfma_scale_f32_16x16x128_f8f6f4 v[158:161], v[2:9], v[184:191], v[158:161], v1, v1 op_sel_hi:[0,0,0]
	v_mfma_scale_f32_16x16x128_f8f6f4 v[154:157], v[10:17], v[184:191], v[154:157], v1, v1 op_sel_hi:[0,0,0]
	v_mfma_scale_f32_16x16x128_f8f6f4 v[142:145], v[2:9], v[196:203], v[142:145], v1, v1 op_sel_hi:[0,0,0]
	v_mfma_scale_f32_16x16x128_f8f6f4 v[138:141], v[10:17], v[196:203], v[138:141], v1, v1 op_sel_hi:[0,0,0]
	v_mfma_scale_f32_16x16x128_f8f6f4 v[126:129], v[2:9], v[204:211], v[126:129], v1, v1 op_sel_hi:[0,0,0]
	v_mfma_scale_f32_16x16x128_f8f6f4 v[122:125], v[10:17], v[204:211], v[122:125], v1, v1 op_sel_hi:[0,0,0]
	v_mfma_scale_f32_16x16x128_f8f6f4 v[110:113], v[2:9], v[212:219], v[110:113], v1, v1 op_sel_hi:[0,0,0]
	v_mfma_scale_f32_16x16x128_f8f6f4 v[106:109], v[10:17], v[212:219], v[106:109], v1, v1 op_sel_hi:[0,0,0]
	s_setprio 0
	s_setprio 1
	v_mfma_scale_f32_16x16x128_f8f6f4 v[150:153], v[18:25], v[184:191], v[150:153], v1, v1 op_sel_hi:[0,0,0]
	v_mfma_scale_f32_16x16x128_f8f6f4 v[146:149], v[26:33], v[184:191], v[146:149], v1, v1 op_sel_hi:[0,0,0]
	v_mfma_scale_f32_16x16x128_f8f6f4 v[134:137], v[18:25], v[196:203], v[134:137], v1, v1 op_sel_hi:[0,0,0]
	v_mfma_scale_f32_16x16x128_f8f6f4 v[130:133], v[26:33], v[196:203], v[130:133], v1, v1 op_sel_hi:[0,0,0]
	v_mfma_scale_f32_16x16x128_f8f6f4 v[118:121], v[18:25], v[204:211], v[118:121], v1, v1 op_sel_hi:[0,0,0]
	v_mfma_scale_f32_16x16x128_f8f6f4 v[114:117], v[26:33], v[204:211], v[114:117], v1, v1 op_sel_hi:[0,0,0]
	v_mfma_scale_f32_16x16x128_f8f6f4 v[102:105], v[18:25], v[212:219], v[102:105], v1, v1 op_sel_hi:[0,0,0]
	v_mfma_scale_f32_16x16x128_f8f6f4 v[98:101], v[26:33], v[212:219], v[98:101], v1, v1 op_sel_hi:[0,0,0]
	s_setprio 0
	s_barrier
	s_add_i32 s62, s85, s60
	v_lshl_add_u64 v[170:171], v[170:171], 0, s[24:25]
	s_mov_b32 m0, s62
	ds_read_b128 v[184:187], v182 offset:49152
	ds_read_b128 v[196:199], v182 offset:51200
	ds_read_b128 v[188:191], v183 offset:49152
	ds_read_b128 v[200:203], v183 offset:51200
	ds_read_b128 v[204:207], v182 offset:53248
	ds_read_b128 v[212:215], v182 offset:55296
	ds_read_b128 v[208:211], v183 offset:53248
	ds_read_b128 v[216:219], v183 offset:55296
	global_load_lds_dwordx4 v[170:171], off
	s_add_i32 m0, s62, 0x2000
	s_add_u32 s34, s34, 0x40080
	v_lshl_add_u64 v[170:171], v[172:173], 0, s[24:25]
	s_addc_u32 s35, s35, 0
	s_add_i32 s62, s86, s60
	global_load_lds_dwordx4 v[170:171], off
	v_lshl_add_u64 v[170:171], s[34:35], 0, v[164:165]
	s_mov_b32 m0, s62
	s_nop 0
	global_load_lds_dwordx4 v[170:171], off
	v_lshl_add_u64 v[170:171], s[34:35], 0, v[168:169]
	s_add_i32 m0, s62, 0x2000
	s_nop 0
	global_load_lds_dwordx4 v[170:171], off
	v_lshl_add_u64 v[170:171], v[174:175], 0, s[24:25]
	s_mov_b32 m0, s80
	s_nop 0
	global_load_lds_dwordx4 v[170:171], off
	s_waitcnt vmcnt(7)
	s_waitcnt lgkmcnt(0)
	s_barrier
	s_setprio 1
	s_waitcnt lgkmcnt(0)
	v_mfma_scale_f32_16x16x128_f8f6f4 v[94:97], v[2:9], v[184:191], v[94:97], v1, v1 op_sel_hi:[0,0,0]
	v_mfma_scale_f32_16x16x128_f8f6f4 v[90:93], v[10:17], v[184:191], v[90:93], v1, v1 op_sel_hi:[0,0,0]
	v_mfma_scale_f32_16x16x128_f8f6f4 v[78:81], v[2:9], v[196:203], v[78:81], v1, v1 op_sel_hi:[0,0,0]
	v_mfma_scale_f32_16x16x128_f8f6f4 v[74:77], v[10:17], v[196:203], v[74:77], v1, v1 op_sel_hi:[0,0,0]
	v_mfma_scale_f32_16x16x128_f8f6f4 v[62:65], v[2:9], v[204:211], v[62:65], v1, v1 op_sel_hi:[0,0,0]
	v_mfma_scale_f32_16x16x128_f8f6f4 v[58:61], v[10:17], v[204:211], v[58:61], v1, v1 op_sel_hi:[0,0,0]
	v_mfma_scale_f32_16x16x128_f8f6f4 v[46:49], v[2:9], v[212:219], v[46:49], v1, v1 op_sel_hi:[0,0,0]
	v_mfma_scale_f32_16x16x128_f8f6f4 v[42:45], v[10:17], v[212:219], v[42:45], v1, v1 op_sel_hi:[0,0,0]
	s_setprio 0
	v_lshl_add_u64 v[170:171], v[176:177], 0, s[24:25]
	s_mov_b32 m0, s81
	s_nop 0
	global_load_lds_dwordx4 v[170:171], off
	s_setprio 1
	v_mfma_scale_f32_16x16x128_f8f6f4 v[86:89], v[18:25], v[184:191], v[86:89], v1, v1 op_sel_hi:[0,0,0]
	v_mfma_scale_f32_16x16x128_f8f6f4 v[82:85], v[26:33], v[184:191], v[82:85], v1, v1 op_sel_hi:[0,0,0]
	v_mfma_scale_f32_16x16x128_f8f6f4 v[70:73], v[18:25], v[196:203], v[70:73], v1, v1 op_sel_hi:[0,0,0]
	v_mfma_scale_f32_16x16x128_f8f6f4 v[66:69], v[26:33], v[196:203], v[66:69], v1, v1 op_sel_hi:[0,0,0]
	v_mfma_scale_f32_16x16x128_f8f6f4 v[54:57], v[18:25], v[204:211], v[54:57], v1, v1 op_sel_hi:[0,0,0]
	v_mfma_scale_f32_16x16x128_f8f6f4 v[50:53], v[26:33], v[204:211], v[50:53], v1, v1 op_sel_hi:[0,0,0]
	v_mfma_scale_f32_16x16x128_f8f6f4 v[38:41], v[18:25], v[212:219], v[38:41], v1, v1 op_sel_hi:[0,0,0]
	v_mfma_scale_f32_16x16x128_f8f6f4 v[34:37], v[26:33], v[212:219], v[34:37], v1, v1 op_sel_hi:[0,0,0]
	s_setprio 0
	s_barrier
	s_cmp_gt_u32 s47, 13
	s_mov_b32 s34, s47
	s_cbranch_scc0 .LBB0_920
	s_and_b64 vcc, exec, s[40:41]
	s_cbranch_vccz .LBB0_923
	s_barrier

; #define PG8_STAGE(bufoff, gbase, voff) do { _Pragma("unroll") for (int _i = 0; _i < 2; ++_i) \
;         __builtin_amdgcn_global_load_lds((const unsigned*)((const char*)(gbase) + (voff)[_i]), (LAS unsigned*)(lds + (bufoff) + ldsw + _i * 8192), 16, 0, 0); } while (0)
; #define PG8_WAIT_V(n) asm volatile("s_waitcnt vmcnt(" #n ")" ::: "memory")
; #define PG8_WAIT_L(n) asm volatile("s_waitcnt lgkmcnt(" #n ")" ::: "memory")
; #define PG8_BAR __builtin_amdgcn_s_barrier()
; #define PG8_SCHED __builtin_amdgcn_sched_barrier(0)
; #define PG8_STA_CUR(buf, kb, h) do { if constexpr (GATHER) { PG8_STAGE(buf, gA + (kb), oc[h]); } else { PG8_STAGE(buf, cA + (kb) + (h) * hstep, voffA); } } while (0)
; template <class Epi, class Sched, bool GATHER, bool F8 = false>
; __device__ __forceinline__ void gemm_phase(LAS unsigned char* lds, const Gemm g, const Sched& S, const Epi& E, const int tid) {
;     ...
;         for (int t = 0; t < nt; t += 2) {
;             const bool last = (t == nt - 2);
;             int to = t; asm volatile("" : "+s"(to));
;             const size_t k1 = (size_t)(to + 1) * kstep, k2 = last ? 0 : (size_t)(to + 2) * kstep, k3 = k2 + kstep;
;             const char* b2 = last ? nB : cB + (size_t)(to + 2) * kstep; const char* b3 = b2 + kstep;
;             const char* a2p = last ? nA : cA;
;             if constexpr (GATHER) { if (last) { if (has_next) { PG8_AOFF(on, nxt); } else {
; #pragma unroll
;                 for (int h = 0; h < 2; ++h)
; #pragma unroll
;                     for (int i = 0; i < 2; ++i) on[h][i] = oc[h][i]; } } }
;             PG8_LDB(B0, 0, 0); PG8_LDB(B1, 0, 1); PG8_SCHED; PG8_LDA(At, 0, 0); PG8_STA_CUR(PG8_SA(1, 1), k1, 1);
;             PG8_WAIT_V(8); PG8_WAIT_L(0); PG8_BAR; PG8_MMA(0, 0, At, B0); PG8_MMA(0, 1, At, B1); PG8_BAR; PG8_SCHED;
;             PG8_LDA(At, 0, 1); PG8_STAGE(PG8_SB(0, 0), b2, voffB); PG8_STAGE(PG8_SB(0, 1), b2 + hstepB, voffB); PG8_STA_SEL(PG8_SA(0, 0), k2, 0);
;             PG8_WAIT_V(8); PG8_WAIT_L(0); PG8_BAR; PG8_MMA(1, 0, At, B0); PG8_MMA(1, 1, At, B1); PG8_BAR; PG8_SCHED;
;             PG8_LDB(B0, 1, 0); PG8_LDB(B1, 1, 1); PG8_SCHED; PG8_LDA(At, 1, 0); PG8_STA_SEL(PG8_SA(0, 1), k2, 1);
;             PG8_WAIT_V(8); PG8_WAIT_L(0); PG8_BAR; PG8_MMA(0, 0, At, B0); PG8_MMA(0, 1, At, B1); PG8_BAR; PG8_SCHED;
.LBB0_1370:
	s_add_i32 s75, s34, 2
	s_mov_b32 s58, s75
	s_ashr_i32 s59, s58, 31
	s_lshl_b64 s[58:59], s[58:59], 7
	s_add_u32 s84, s58, 0x100
	s_addc_u32 s81, s59, 0
	s_add_u32 s85, s54, s84
	s_addc_u32 s88, s55, s81
	s_add_i32 s80, 0, 0x10000
	s_cmp_eq_u32 s34, 4
	s_cselect_b64 s[86:87], -1, 0
	s_and_b64 s[34:35], s[86:87], exec
	s_cselect_b32 s35, s43, s88
	s_cselect_b32 s34, s45, s85
	s_cselect_b32 s81, 0, s81
	s_cselect_b32 s84, 0, s84
	s_and_b64 s[86:87], s[48:49], s[86:87]
	s_and_b64 s[86:87], s[86:87], exec
	s_cselect_b32 s85, s47, s57
	s_cselect_b32 s86, s46, s56
	s_add_i32 s87, 0, 0x14000
	v_add_u32_e32 v2, s80, v179
	v_add_u32_e32 v3, s80, v180
	v_add_u32_e32 v6, s87, v179
	v_add_u32_e32 v14, s87, v180
	ds_read_b128 v[18:21], v2
	ds_read_b128 v[26:29], v2 offset:2048
	ds_read_b128 v[22:25], v3
	ds_read_b128 v[30:33], v3 offset:2048
	ds_read_b128 v[2:5], v6
	ds_read_b128 v[10:13], v6 offset:2048
	ds_read_b128 v[6:9], v14
	ds_read_b128 v[14:17], v14 offset:2048
	s_add_u32 s58, s56, s58
	s_addc_u32 s59, s57, s59
	s_add_u32 s58, s58, 0x20080
	s_addc_u32 s59, s59, 0
	v_lshl_add_u64 v[192:193], s[58:59], 0, v[162:163]
	s_add_i32 m0, s53, 0xc000
	ds_read_b128 v[170:173], v182
	ds_read_b128 v[184:187], v182 offset:2048
	ds_read_b128 v[174:177], v183
	ds_read_b128 v[188:191], v183 offset:2048
	ds_read_b128 v[196:199], v182 offset:4096
	ds_read_b128 v[204:207], v182 offset:6144
	ds_read_b128 v[200:203], v183 offset:4096
	ds_read_b128 v[208:211], v183 offset:6144
	global_load_lds_dwordx4 v[192:193], off
	v_lshl_add_u64 v[192:193], s[58:59], 0, v[166:167]
	s_add_i32 m0, s53, 0xe000
	s_nop 0
	global_load_lds_dwordx4 v[192:193], off
	s_waitcnt vmcnt(8)
	s_waitcnt lgkmcnt(0)
	s_barrier
	s_setprio 1
	s_waitcnt lgkmcnt(0)
	v_mfma_scale_f32_16x16x128_f8f6f4 v[158:161], v[18:25], v[170:177], v[158:161], v1, v1 op_sel_hi:[0,0,0]
	v_mfma_scale_f32_16x16x128_f8f6f4 v[154:157], v[26:33], v[170:177], v[154:157], v1, v1 op_sel_hi:[0,0,0]
	v_mfma_scale_f32_16x16x128_f8f6f4 v[142:145], v[18:25], v[184:191], v[142:145], v1, v1 op_sel_hi:[0,0,0]
	v_mfma_scale_f32_16x16x128_f8f6f4 v[138:141], v[26:33], v[184:191], v[138:141], v1, v1 op_sel_hi:[0,0,0]
	v_mfma_scale_f32_16x16x128_f8f6f4 v[126:129], v[18:25], v[196:203], v[126:129], v1, v1 op_sel_hi:[0,0,0]
	v_mfma_scale_f32_16x16x128_f8f6f4 v[122:125], v[26:33], v[196:203], v[122:125], v1, v1 op_sel_hi:[0,0,0]
	v_mfma_scale_f32_16x16x128_f8f6f4 v[110:113], v[18:25], v[204:211], v[110:113], v1, v1 op_sel_hi:[0,0,0]
	v_mfma_scale_f32_16x16x128_f8f6f4 v[106:109], v[26:33], v[204:211], v[106:109], v1, v1 op_sel_hi:[0,0,0]
	s_setprio 0
	s_setprio 1
	v_mfma_scale_f32_16x16x128_f8f6f4 v[150:153], v[2:9], v[170:177], v[150:153], v1, v1 op_sel_hi:[0,0,0]
	v_mfma_scale_f32_16x16x128_f8f6f4 v[146:149], v[10:17], v[170:177], v[146:149], v1, v1 op_sel_hi:[0,0,0]
	v_mfma_scale_f32_16x16x128_f8f6f4 v[134:137], v[2:9], v[184:191], v[134:137], v1, v1 op_sel_hi:[0,0,0]
	v_mfma_scale_f32_16x16x128_f8f6f4 v[130:133], v[10:17], v[184:191], v[130:133], v1, v1 op_sel_hi:[0,0,0]
	v_mfma_scale_f32_16x16x128_f8f6f4 v[118:121], v[2:9], v[196:203], v[118:121], v1, v1 op_sel_hi:[0,0,0]
	v_mfma_scale_f32_16x16x128_f8f6f4 v[114:117], v[10:17], v[196:203], v[114:117], v1, v1 op_sel_hi:[0,0,0]
	v_mfma_scale_f32_16x16x128_f8f6f4 v[102:105], v[2:9], v[204:211], v[102:105], v1, v1 op_sel_hi:[0,0,0]
	v_mfma_scale_f32_16x16x128_f8f6f4 v[98:101], v[10:17], v[204:211], v[98:101], v1, v1 op_sel_hi:[0,0,0]
	s_setprio 0
	s_barrier
	s_add_i32 s58, s80, s62
	v_lshl_add_u64 v[170:171], s[34:35], 0, v[164:165]
	s_mov_b32 m0, s58
	ds_read_b128 v[184:187], v182 offset:16384
	ds_read_b128 v[196:199], v182 offset:18432
	ds_read_b128 v[188:191], v183 offset:16384
	ds_read_b128 v[200:203], v183 offset:18432
	ds_read_b128 v[204:207], v182 offset:20480
	ds_read_b128 v[212:215], v182 offset:22528
	ds_read_b128 v[208:211], v183 offset:20480
	ds_read_b128 v[216:219], v183 offset:22528
	global_load_lds_dwordx4 v[170:171], off
	s_add_i32 m0, s58, 0x2000
	s_add_u32 s58, s34, 0x20000
	v_lshl_add_u64 v[172:173], s[34:35], 0, v[168:169]
	s_addc_u32 s59, s35, 0
	s_add_i32 s80, s87, s62
	global_load_lds_dwordx4 v[172:173], off
	v_lshl_add_u64 v[174:175], s[58:59], 0, v[164:165]
	s_mov_b32 m0, s80
	s_nop 0
	global_load_lds_dwordx4 v[174:175], off
	s_add_i32 m0, s80, 0x2000
	v_lshl_add_u64 v[174:175], s[58:59], 0, v[168:169]
	s_add_u32 s58, s86, s84
	s_addc_u32 s59, s85, s81
	global_load_lds_dwordx4 v[174:175], off
	v_lshl_add_u64 v[174:175], s[58:59], 0, v[162:163]
	s_mov_b32 m0, s53
	v_lshl_add_u64 v[176:177], s[58:59], 0, v[166:167]
	global_load_lds_dwordx4 v[174:175], off
	s_waitcnt vmcnt(7)
	s_waitcnt lgkmcnt(0)
	s_barrier
	s_setprio 1
	s_waitcnt lgkmcnt(0)
	v_mfma_scale_f32_16x16x128_f8f6f4 v[94:97], v[18:25], v[184:191], v[94:97], v1, v1 op_sel_hi:[0,0,0]
	v_mfma_scale_f32_16x16x128_f8f6f4 v[90:93], v[26:33], v[184:191], v[90:93], v1, v1 op_sel_hi:[0,0,0]
	v_mfma_scale_f32_16x16x128_f8f6f4 v[78:81], v[18:25], v[196:203], v[78:81], v1, v1 op_sel_hi:[0,0,0]
	v_mfma_scale_f32_16x16x128_f8f6f4 v[74:77], v[26:33], v[196:203], v[74:77], v1, v1 op_sel_hi:[0,0,0]
	v_mfma_scale_f32_16x16x128_f8f6f4 v[62:65], v[18:25], v[204:211], v[62:65], v1, v1 op_sel_hi:[0,0,0]
	v_mfma_scale_f32_16x16x128_f8f6f4 v[58:61], v[26:33], v[204:211], v[58:61], v1, v1 op_sel_hi:[0,0,0]
	v_mfma_scale_f32_16x16x128_f8f6f4 v[46:49], v[18:25], v[212:219], v[46:49], v1, v1 op_sel_hi:[0,0,0]
	v_mfma_scale_f32_16x16x128_f8f6f4 v[42:45], v[26:33], v[212:219], v[42:45], v1, v1 op_sel_hi:[0,0,0]
	s_setprio 0
	s_mov_b32 m0, s4
	s_nop 0
	global_load_lds_dwordx4 v[176:177], off
	s_setprio 1
	v_mfma_scale_f32_16x16x128_f8f6f4 v[86:89], v[2:9], v[184:191], v[86:89], v1, v1 op_sel_hi:[0,0,0]
	v_mfma_scale_f32_16x16x128_f8f6f4 v[82:85], v[10:17], v[184:191], v[82:85], v1, v1 op_sel_hi:[0,0,0]
	v_mfma_scale_f32_16x16x128_f8f6f4 v[70:73], v[2:9], v[196:203], v[70:73], v1, v1 op_sel_hi:[0,0,0]
	v_mfma_scale_f32_16x16x128_f8f6f4 v[66:69], v[10:17], v[196:203], v[66:69], v1, v1 op_sel_hi:[0,0,0]
	v_mfma_scale_f32_16x16x128_f8f6f4 v[54:57], v[2:9], v[204:211], v[54:57], v1, v1 op_sel_hi:[0,0,0]
	v_mfma_scale_f32_16x16x128_f8f6f4 v[50:53], v[10:17], v[204:211], v[50:53], v1, v1 op_sel_hi:[0,0,0]
	v_mfma_scale_f32_16x16x128_f8f6f4 v[38:41], v[2:9], v[212:219], v[38:41], v1, v1 op_sel_hi:[0,0,0]
	v_mfma_scale_f32_16x16x128_f8f6f4 v[34:37], v[10:17], v[212:219], v[34:37], v1, v1 op_sel_hi:[0,0,0]
	s_setprio 0
	s_barrier
; #define PG8_STAGE(bufoff, gbase, voff) do { _Pragma("unroll") for (int _i = 0; _i < 2; ++_i) \
;         __builtin_amdgcn_global_load_lds((const unsigned*)((const char*)(gbase) + (voff)[_i]), (LAS unsigned*)(lds + (bufoff) + ldsw + _i * 8192), 16, 0, 0); } while (0)
; #define PG8_WAIT_V(n) asm volatile("s_waitcnt vmcnt(" #n ")" ::: "memory")
; #define PG8_WAIT_L(n) asm volatile("s_waitcnt lgkmcnt(" #n ")" ::: "memory")
; #define PG8_BAR __builtin_amdgcn_s_barrier()
; #define PG8_SCHED __builtin_amdgcn_sched_barrier(0)
; #define PG8_STA_SEL(buf, kb, h) do { if constexpr (GATHER) { if (last) { PG8_STAGE(buf, gA + (kb), on[h]); } else { PG8_STAGE(buf, gA + (kb), oc[h]); } } else { PG8_STAGE(buf, a2p + (kb) + (h) * hstep, voffA); } } while (0)
; template <class Epi, class Sched, bool GATHER, bool F8 = false>
; __device__ __forceinline__ void gemm_phase(LAS unsigned char* lds, const Gemm g, const Sched& S, const Epi& E, const int tid) {
;     ...
;             PG8_LDB(B0, 1, 0); PG8_LDB(B1, 1, 1); PG8_SCHED; PG8_LDA(At, 1, 0); PG8_STA_SEL(PG8_SA(0, 1), k2, 1);
;             PG8_WAIT_V(8); PG8_WAIT_L(0); PG8_BAR; PG8_MMA(0, 0, At, B0); PG8_MMA(0, 1, At, B1); PG8_BAR; PG8_SCHED;
;             PG8_LDA(At, 1, 1); PG8_STAGE(PG8_SB(1, 0), b3, voffB); PG8_STAGE(PG8_SB(1, 1), b3 + hstepB, voffB); PG8_STA_SEL(PG8_SA(1, 0), k3, 0);
;             PG8_WAIT_V(8); PG8_WAIT_L(0); PG8_BAR; PG8_MMA(1, 0, At, B0); PG8_MMA(1, 1, At, B1); PG8_BAR; PG8_SCHED;
;         }
;         if (wr == 0) PG8_BAR;
	s_add_i32 s80, 0, 0x18000
	s_add_i32 s81, 0, 0x1c000
	v_add_u32_e32 v6, s80, v179
	v_add_u32_e32 v14, s80, v180
	v_add_u32_e32 v22, s81, v179
	v_add_u32_e32 v30, s81, v180
	ds_read_b128 v[2:5], v6
	ds_read_b128 v[10:13], v6 offset:2048
	ds_read_b128 v[6:9], v14
	ds_read_b128 v[14:17], v14 offset:2048
	ds_read_b128 v[18:21], v22
	ds_read_b128 v[26:29], v22 offset:2048
	ds_read_b128 v[22:25], v30
	ds_read_b128 v[30:33], v30 offset:2048
	s_add_u32 s58, s58, 0x20000
	s_addc_u32 s59, s59, 0
	s_mov_b32 m0, s5
	v_lshl_add_u64 v[192:193], s[58:59], 0, v[162:163]
	ds_read_b128 v[184:187], v182 offset:32768
	ds_read_b128 v[196:199], v182 offset:34816
	ds_read_b128 v[188:191], v183 offset:32768
	ds_read_b128 v[200:203], v183 offset:34816
	ds_read_b128 v[204:207], v182 offset:36864
	ds_read_b128 v[212:215], v182 offset:38912
	ds_read_b128 v[208:211], v183 offset:36864
	ds_read_b128 v[216:219], v183 offset:38912
	global_load_lds_dwordx4 v[192:193], off
	v_lshl_add_u64 v[192:193], s[58:59], 0, v[166:167]
	s_mov_b32 m0, s63
	s_nop 0
	global_load_lds_dwordx4 v[192:193], off
	s_waitcnt vmcnt(8)
	s_waitcnt lgkmcnt(0)
	s_barrier
	s_setprio 1
	s_waitcnt lgkmcnt(0)
	v_mfma_scale_f32_16x16x128_f8f6f4 v[158:161], v[2:9], v[184:191], v[158:161], v1, v1 op_sel_hi:[0,0,0]
	v_mfma_scale_f32_16x16x128_f8f6f4 v[154:157], v[10:17], v[184:191], v[154:157], v1, v1 op_sel_hi:[0,0,0]
	v_mfma_scale_f32_16x16x128_f8f6f4 v[142:145], v[2:9], v[196:203], v[142:145], v1, v1 op_sel_hi:[0,0,0]
	v_mfma_scale_f32_16x16x128_f8f6f4 v[138:141], v[10:17], v[196:203], v[138:141], v1, v1 op_sel_hi:[0,0,0]
	v_mfma_scale_f32_16x16x128_f8f6f4 v[126:129], v[2:9], v[204:211], v[126:129], v1, v1 op_sel_hi:[0,0,0]
	v_mfma_scale_f32_16x16x128_f8f6f4 v[122:125], v[10:17], v[204:211], v[122:125], v1, v1 op_sel_hi:[0,0,0]
	v_mfma_scale_f32_16x16x128_f8f6f4 v[110:113], v[2:9], v[212:219], v[110:113], v1, v1 op_sel_hi:[0,0,0]
	v_mfma_scale_f32_16x16x128_f8f6f4 v[106:109], v[10:17], v[212:219], v[106:109], v1, v1 op_sel_hi:[0,0,0]
	s_setprio 0
	s_setprio 1
	v_mfma_scale_f32_16x16x128_f8f6f4 v[150:153], v[18:25], v[184:191], v[150:153], v1, v1 op_sel_hi:[0,0,0]
	v_mfma_scale_f32_16x16x128_f8f6f4 v[146:149], v[26:33], v[184:191], v[146:149], v1, v1 op_sel_hi:[0,0,0]
	v_mfma_scale_f32_16x16x128_f8f6f4 v[134:137], v[18:25], v[196:203], v[134:137], v1, v1 op_sel_hi:[0,0,0]
	v_mfma_scale_f32_16x16x128_f8f6f4 v[130:133], v[26:33], v[196:203], v[130:133], v1, v1 op_sel_hi:[0,0,0]
	v_mfma_scale_f32_16x16x128_f8f6f4 v[118:121], v[18:25], v[204:211], v[118:121], v1, v1 op_sel_hi:[0,0,0]
	v_mfma_scale_f32_16x16x128_f8f6f4 v[114:117], v[26:33], v[204:211], v[114:117], v1, v1 op_sel_hi:[0,0,0]
	v_mfma_scale_f32_16x16x128_f8f6f4 v[102:105], v[18:25], v[212:219], v[102:105], v1, v1 op_sel_hi:[0,0,0]
	v_mfma_scale_f32_16x16x128_f8f6f4 v[98:101], v[26:33], v[212:219], v[98:101], v1, v1 op_sel_hi:[0,0,0]
	s_setprio 0
	s_barrier
	s_add_i32 s58, s80, s62
	v_lshl_add_u64 v[170:171], v[170:171], 0, s[24:25]
	s_mov_b32 m0, s58
	ds_read_b128 v[184:187], v182 offset:49152
	ds_read_b128 v[196:199], v182 offset:51200
	ds_read_b128 v[188:191], v183 offset:49152
	ds_read_b128 v[200:203], v183 offset:51200
	ds_read_b128 v[204:207], v182 offset:53248
	ds_read_b128 v[212:215], v182 offset:55296
	ds_read_b128 v[208:211], v183 offset:53248
	ds_read_b128 v[216:219], v183 offset:55296
	global_load_lds_dwordx4 v[170:171], off
	s_add_i32 m0, s58, 0x2000
	s_add_u32 s34, s34, 0x20080
	v_lshl_add_u64 v[170:171], v[172:173], 0, s[24:25]
	s_addc_u32 s35, s35, 0
	s_add_i32 s58, s81, s62
	global_load_lds_dwordx4 v[170:171], off
	v_lshl_add_u64 v[170:171], s[34:35], 0, v[164:165]
	s_mov_b32 m0, s58
	s_nop 0
	global_load_lds_dwordx4 v[170:171], off
	v_lshl_add_u64 v[170:171], s[34:35], 0, v[168:169]
	s_add_i32 m0, s58, 0x2000
	s_nop 0
	global_load_lds_dwordx4 v[170:171], off
	v_lshl_add_u64 v[170:171], v[174:175], 0, s[24:25]
	s_mov_b32 m0, s72
	s_nop 0
	global_load_lds_dwordx4 v[170:171], off
	s_waitcnt vmcnt(7)
	s_waitcnt lgkmcnt(0)
	s_barrier
	s_setprio 1
	s_waitcnt lgkmcnt(0)
	v_mfma_scale_f32_16x16x128_f8f6f4 v[94:97], v[2:9], v[184:191], v[94:97], v1, v1 op_sel_hi:[0,0,0]
	v_mfma_scale_f32_16x16x128_f8f6f4 v[90:93], v[10:17], v[184:191], v[90:93], v1, v1 op_sel_hi:[0,0,0]
	v_mfma_scale_f32_16x16x128_f8f6f4 v[78:81], v[2:9], v[196:203], v[78:81], v1, v1 op_sel_hi:[0,0,0]
	v_mfma_scale_f32_16x16x128_f8f6f4 v[74:77], v[10:17], v[196:203], v[74:77], v1, v1 op_sel_hi:[0,0,0]
	v_mfma_scale_f32_16x16x128_f8f6f4 v[62:65], v[2:9], v[204:211], v[62:65], v1, v1 op_sel_hi:[0,0,0]
	v_mfma_scale_f32_16x16x128_f8f6f4 v[58:61], v[10:17], v[204:211], v[58:61], v1, v1 op_sel_hi:[0,0,0]
	v_mfma_scale_f32_16x16x128_f8f6f4 v[46:49], v[2:9], v[212:219], v[46:49], v1, v1 op_sel_hi:[0,0,0]
	v_mfma_scale_f32_16x16x128_f8f6f4 v[42:45], v[10:17], v[212:219], v[42:45], v1, v1 op_sel_hi:[0,0,0]
	s_setprio 0
	v_lshl_add_u64 v[170:171], v[176:177], 0, s[24:25]
	s_mov_b32 m0, s73
	s_nop 0
	global_load_lds_dwordx4 v[170:171], off
	s_setprio 1
	v_mfma_scale_f32_16x16x128_f8f6f4 v[86:89], v[18:25], v[184:191], v[86:89], v1, v1 op_sel_hi:[0,0,0]
	v_mfma_scale_f32_16x16x128_f8f6f4 v[82:85], v[26:33], v[184:191], v[82:85], v1, v1 op_sel_hi:[0,0,0]
	v_mfma_scale_f32_16x16x128_f8f6f4 v[70:73], v[18:25], v[196:203], v[70:73], v1, v1 op_sel_hi:[0,0,0]
	v_mfma_scale_f32_16x16x128_f8f6f4 v[66:69], v[26:33], v[196:203], v[66:69], v1, v1 op_sel_hi:[0,0,0]
	v_mfma_scale_f32_16x16x128_f8f6f4 v[54:57], v[18:25], v[204:211], v[54:57], v1, v1 op_sel_hi:[0,0,0]
	v_mfma_scale_f32_16x16x128_f8f6f4 v[50:53], v[26:33], v[204:211], v[50:53], v1, v1 op_sel_hi:[0,0,0]
	v_mfma_scale_f32_16x16x128_f8f6f4 v[38:41], v[18:25], v[212:219], v[38:41], v1, v1 op_sel_hi:[0,0,0]
	v_mfma_scale_f32_16x16x128_f8f6f4 v[34:37], v[26:33], v[212:219], v[34:37], v1, v1 op_sel_hi:[0,0,0]
	s_setprio 0
	s_barrier
	s_cmp_gt_u32 s75, 5
	s_mov_b32 s34, s75
	s_cbranch_scc0 .LBB0_1370
	s_and_b64 vcc, exec, s[40:41]
	s_cbranch_vccz .LBB0_1373
	s_barrier
